# P0 norm rows: g_mix vectors loaded once, 15 reload+vmcnt(0) round trips removed (on top of P2 rewrite + conv waits)
# speedup vs baseline: 1.0203x; 1.0052x over previous
; __device__ __forceinline__ unsigned pk2(float lo, float hi) { return (unsigned)f2bf(lo) | ((unsigned)f2bf(hi) << 16); }
; __device__ __forceinline__ float wave_sum(float v) {
; #pragma unroll
;     for (int o = 1; o < 64; o <<= 1) v += __shfl_xor(v, o);
;     return v;
; }
; __device__ __forceinline__ void norm1_rows2(int R0, int lane, const float* x, const float* meta, const float* g, bf16* hn) {
;     f32x4 v[2][8]; float ss[2] = {0.f, 0.f};
; #pragma unroll
;     for (int q = 0; q < 2; ++q) { const int R = R0 + q; const float* src = R < M ? x + (size_t)R * D : meta + (size_t)(R - M) * D;
; #pragma unroll
;         for (int j = 0; j < 8; ++j) v[q][j] = __builtin_nontemporal_load((const f32x4*)(src + j * 256 + lane * 4)); }
; #pragma unroll
;     for (int q = 0; q < 2; ++q)
; #pragma unroll
;         for (int j = 0; j < 8; ++j) ss[q] += v[q][j].x * v[q][j].x + v[q][j].y * v[q][j].y + v[q][j].z * v[q][j].z + v[q][j].w * v[q][j].w;
; #pragma unroll
;     for (int q = 0; q < 2; ++q) { const float rstd = rsqrtf(wave_sum(ss[q]) * (1.f / D) + EPS);
; #pragma unroll
;         for (int j = 0; j < 8; ++j) { const f32x4 gg = *(const f32x4*)(g + j * 256 + lane * 4);
;             u32x2 o; o.x = pk2(v[q][j].x * rstd * gg.x, v[q][j].y * rstd * gg.y); o.y = pk2(v[q][j].z * rstd * gg.z, v[q][j].w * rstd * gg.w);
;             *(u32x2*)(hn + (size_t)(R0 + q) * D + j * 256 + lane * 4) = o; } }
; }
.LBB0_45:
	v_lshl_add_u64 v[2:3], s[10:11], 0, v[72:73]
	v_add_co_u32_e32 v2, vcc, 0x1000, v2
	global_load_dwordx4 v[30:33], v72, s[10:11] nt
	global_load_dwordx4 v[26:29], v72, s[10:11] offset:1024 nt
	global_load_dwordx4 v[22:25], v72, s[10:11] offset:2048 nt
	global_load_dwordx4 v[18:21], v72, s[10:11] offset:3072 nt
	v_addc_co_u32_e32 v3, vcc, 0, v3, vcc
	global_load_dwordx4 v[14:17], v[2:3], off nt
	global_load_dwordx4 v[10:13], v[2:3], off offset:1024 nt
	global_load_dwordx4 v[6:9], v[2:3], off offset:2048 nt
	s_nop 0
	global_load_dwordx4 v[2:5], v[2:3], off offset:3072 nt
	s_waitcnt vmcnt(11)
	v_mov_b32_e32 v68, v47
	s_waitcnt lgkmcnt(0)
	global_load_dwordx4 v[118:121], v72, s[6:7]
	s_waitcnt vmcnt(11)
	v_mov_b32_e32 v69, v43
	v_mov_b32_e32 v66, v46
	v_mov_b32_e32 v67, v42
	v_pk_mul_f32 v[68:69], v[68:69], v[68:69]
	v_mov_b32_e32 v99, v59
	v_pk_fma_f32 v[66:67], v[66:67], v[66:67], v[68:69]
	v_mov_b32_e32 v68, v48
	v_mov_b32_e32 v69, v44
	v_pk_fma_f32 v[66:67], v[68:69], v[68:69], v[66:67]
	v_mov_b32_e32 v68, v49
	v_mov_b32_e32 v69, v45
	v_pk_fma_f32 v[92:93], v[68:69], v[68:69], v[66:67]
	s_waitcnt vmcnt(10)
	v_mov_b32_e32 v68, v39
	s_waitcnt vmcnt(9)
	v_mov_b32_e32 v69, v35
	v_mov_b32_e32 v66, v38
	v_mov_b32_e32 v67, v34
	v_pk_mul_f32 v[68:69], v[68:69], v[68:69]
	v_mov_b32_e32 v122, v62
	v_pk_fma_f32 v[66:67], v[66:67], v[66:67], v[68:69]
	v_mov_b32_e32 v68, v40
	v_mov_b32_e32 v69, v36
	v_pk_fma_f32 v[66:67], v[68:69], v[68:69], v[66:67]
	v_mov_b32_e32 v68, v41
	v_mov_b32_e32 v69, v37
	v_pk_fma_f32 v[94:95], v[68:69], v[68:69], v[66:67]
	v_mov_b32_e32 v123, v64
	s_add_i32 s40, s54, 0xff320000
	s_waitcnt vmcnt(7)
	v_mov_b32_e32 v98, v27
	v_pk_mul_f32 v[98:99], v[98:99], v[98:99]
	s_waitcnt vmcnt(4)
	v_mov_b32_e32 v68, v15
	s_waitcnt vmcnt(3)
	v_mov_b32_e32 v69, v11
	v_mov_b32_e32 v66, v14
	v_mov_b32_e32 v67, v10
	v_pk_mul_f32 v[68:69], v[68:69], v[68:69]
	s_waitcnt vmcnt(0)
	v_add_u32_e32 v164, 0x1000, v72
	global_load_dwordx4 v[132:135], v72, s[6:7]
	global_load_dwordx4 v[136:139], v72, s[6:7] offset:1024
	global_load_dwordx4 v[140:143], v72, s[6:7] offset:2048
	global_load_dwordx4 v[144:147], v72, s[6:7] offset:3072
	global_load_dwordx4 v[148:151], v164, s[6:7]
	global_load_dwordx4 v[152:155], v164, s[6:7] offset:1024
	global_load_dwordx4 v[156:159], v164, s[6:7] offset:2048
	global_load_dwordx4 v[160:163], v164, s[6:7] offset:3072
	v_mov_b32_e32 v124, v118
	v_pk_fma_f32 v[66:67], v[66:67], v[66:67], v[68:69]
	v_mov_b32_e32 v68, v16
	v_mov_b32_e32 v69, v12
	v_pk_fma_f32 v[66:67], v[68:69], v[68:69], v[66:67]
	v_mov_b32_e32 v68, v17
	v_mov_b32_e32 v69, v13
	v_pk_fma_f32 v[96:97], v[68:69], v[68:69], v[66:67]
	v_mov_b32_e32 v68, v31
	v_mov_b32_e32 v69, v63
	v_mov_b32_e32 v66, v30
	v_mov_b32_e32 v67, v62
	v_pk_mul_f32 v[68:69], v[68:69], v[68:69]
	v_mov_b32_e32 v125, v120
	v_pk_fma_f32 v[66:67], v[66:67], v[66:67], v[68:69]
	v_mov_b32_e32 v68, v32
	v_mov_b32_e32 v69, v64
	v_pk_fma_f32 v[66:67], v[68:69], v[68:69], v[66:67]
	v_mov_b32_e32 v68, v33
	v_mov_b32_e32 v69, v65
	v_pk_fma_f32 v[66:67], v[68:69], v[68:69], v[66:67]
	v_mov_b32_e32 v68, v26
	v_mov_b32_e32 v69, v58
	v_pk_fma_f32 v[68:69], v[68:69], v[68:69], v[98:99]
	v_mov_b32_e32 v98, v28
	v_mov_b32_e32 v99, v60
	v_pk_fma_f32 v[68:69], v[98:99], v[98:99], v[68:69]
	v_mov_b32_e32 v98, v29
	v_mov_b32_e32 v99, v61
	v_pk_fma_f32 v[68:69], v[98:99], v[98:99], v[68:69]
	v_mov_b32_e32 v98, v23
	v_mov_b32_e32 v99, v55
	v_pk_add_f32 v[66:67], v[66:67], v[68:69]
	v_mov_b32_e32 v68, v22
	v_mov_b32_e32 v69, v54
	v_pk_mul_f32 v[98:99], v[98:99], v[98:99]
	v_mov_b32_e32 v120, v119
	v_pk_fma_f32 v[68:69], v[68:69], v[68:69], v[98:99]
	v_mov_b32_e32 v98, v24
	v_mov_b32_e32 v99, v56
	v_pk_fma_f32 v[68:69], v[98:99], v[98:99], v[68:69]
	v_mov_b32_e32 v98, v25
	v_mov_b32_e32 v99, v57
	v_pk_fma_f32 v[68:69], v[98:99], v[98:99], v[68:69]
	v_mov_b32_e32 v98, v19
	v_mov_b32_e32 v99, v51
	v_pk_add_f32 v[66:67], v[66:67], v[68:69]
	v_mov_b32_e32 v68, v18
	v_mov_b32_e32 v69, v50
	v_pk_mul_f32 v[98:99], v[98:99], v[98:99]
	v_mov_b32_e32 v118, v58
	v_pk_fma_f32 v[68:69], v[68:69], v[68:69], v[98:99]
	v_mov_b32_e32 v98, v20
	v_mov_b32_e32 v99, v52
	v_pk_fma_f32 v[68:69], v[98:99], v[98:99], v[68:69]
	v_mov_b32_e32 v98, v21
	v_mov_b32_e32 v99, v53
	v_pk_fma_f32 v[68:69], v[98:99], v[98:99], v[68:69]
	v_mov_b32_e32 v119, v60
	v_pk_add_f32 v[66:67], v[66:67], v[68:69]
	v_mov_b32_e32 v68, v96
	v_mov_b32_e32 v69, v92
	v_pk_add_f32 v[100:101], v[66:67], v[68:69]
	v_mov_b32_e32 v68, v7
	v_mov_b32_e32 v69, v3
	v_mov_b32_e32 v66, v6
	v_mov_b32_e32 v67, v2
	v_pk_mul_f32 v[68:69], v[68:69], v[68:69]
	v_mov_b32_e32 v92, v97
	v_pk_fma_f32 v[66:67], v[66:67], v[66:67], v[68:69]
	v_mov_b32_e32 v68, v8
	v_mov_b32_e32 v69, v4
	v_pk_fma_f32 v[66:67], v[68:69], v[68:69], v[66:67]
	v_mov_b32_e32 v68, v9
	v_mov_b32_e32 v69, v5
	v_pk_fma_f32 v[102:103], v[68:69], v[68:69], v[66:67]
	v_and_b32_e32 v66, 64, v112
	v_add_u32_e32 v66, 64, v66
	v_xor_b32_e32 v67, 1, v112
	v_cmp_lt_i32_e32 vcc, v67, v66
	v_mov_b32_e32 v60, v59
	v_mov_b32_e32 v98, v54
	v_mov_b32_e32 v99, v56
	v_mov_b32_e32 v56, v55
	v_mov_b32_e32 v58, v50
	v_mov_b32_e32 v59, v52
	v_mov_b32_e32 v52, v51
	v_mov_b32_e32 v50, v46
	v_mov_b32_e32 v51, v48
	v_mov_b32_e32 v48, v47
	v_mov_b32_e32 v46, v42
	v_mov_b32_e32 v47, v44
	v_mov_b32_e32 v44, v43
	v_mov_b32_e32 v42, v38
	v_mov_b32_e32 v43, v40
	v_mov_b32_e32 v40, v39
	v_mov_b32_e32 v38, v34
	v_mov_b32_e32 v39, v36
	v_mov_b32_e32 v36, v35
	v_pk_add_f32 v[34:35], v[100:101], v[92:93]
	v_mov_b32_e32 v54, v102
	v_mov_b32_e32 v55, v94
	v_cndmask_b32_e32 v67, v112, v67, vcc
	v_pk_add_f32 v[34:35], v[34:35], v[54:55]
	v_mov_b32_e32 v94, v103
	v_lshlrev_b32_e32 v96, 2, v67
	v_pk_add_f32 v[34:35], v[34:35], v[94:95]
	ds_bpermute_b32 v55, v96, v35
	ds_bpermute_b32 v54, v96, v34
	v_xor_b32_e32 v67, 2, v112
	v_cmp_lt_i32_e32 vcc, v67, v66
	v_mov_b32_e32 v64, v63
	v_lshl_add_u64 v[68:69], s[6:7], 0, v[72:73]
	v_cndmask_b32_e32 v67, v112, v67, vcc
	v_lshlrev_b32_e32 v126, 2, v67
	s_waitcnt lgkmcnt(0)
; __device__ __forceinline__ unsigned pk2(float lo, float hi) { return (unsigned)f2bf(lo) | ((unsigned)f2bf(hi) << 16); }
; __device__ __forceinline__ float wave_sum(float v) {
; #pragma unroll
;     for (int o = 1; o < 64; o <<= 1) v += __shfl_xor(v, o);
;     return v;
; }
; __device__ __forceinline__ void norm1_rows2(int R0, int lane, const float* x, const float* meta, const float* g, bf16* hn) {
;     ...
;     for (int q = 0; q < 2; ++q) { const float rstd = rsqrtf(wave_sum(ss[q]) * (1.f / D) + EPS);
; #pragma unroll
;         for (int j = 0; j < 8; ++j) { const f32x4 gg = *(const f32x4*)(g + j * 256 + lane * 4);
;             u32x2 o; o.x = pk2(v[q][j].x * rstd * gg.x, v[q][j].y * rstd * gg.y); o.y = pk2(v[q][j].z * rstd * gg.z, v[q][j].w * rstd * gg.w);
;             *(u32x2*)(hn + (size_t)(R0 + q) * D + j * 256 + lane * 4) = o; } }
	v_pk_add_f32 v[34:35], v[34:35], v[54:55]
	ds_bpermute_b32 v55, v126, v35
	ds_bpermute_b32 v54, v126, v34
	v_xor_b32_e32 v67, 4, v112
	v_cmp_lt_i32_e32 vcc, v67, v66
	s_waitcnt lgkmcnt(0)
	v_pk_add_f32 v[34:35], v[34:35], v[54:55]
	v_cndmask_b32_e32 v67, v112, v67, vcc
	v_lshlrev_b32_e32 v127, 2, v67
	ds_bpermute_b32 v55, v127, v35
	ds_bpermute_b32 v54, v127, v34
	v_xor_b32_e32 v67, 8, v112
	v_cmp_lt_i32_e32 vcc, v67, v66
	s_waitcnt lgkmcnt(0)
	v_pk_add_f32 v[34:35], v[34:35], v[54:55]
	v_cndmask_b32_e32 v67, v112, v67, vcc
	v_lshlrev_b32_e32 v128, 2, v67
	ds_bpermute_b32 v55, v128, v35
	ds_bpermute_b32 v54, v128, v34
	v_xor_b32_e32 v67, 16, v112
	v_cmp_lt_i32_e32 vcc, v67, v66
	s_waitcnt lgkmcnt(0)
	v_pk_add_f32 v[34:35], v[34:35], v[54:55]
	v_cndmask_b32_e32 v67, v112, v67, vcc
	v_lshlrev_b32_e32 v129, 2, v67
	ds_bpermute_b32 v55, v129, v35
	ds_bpermute_b32 v54, v129, v34
	v_xor_b32_e32 v67, 32, v112
	v_cmp_lt_i32_e32 vcc, v67, v66
	s_waitcnt lgkmcnt(0)
	v_pk_add_f32 v[34:35], v[34:35], v[54:55]
	v_cndmask_b32_e32 v66, v112, v67, vcc
	v_lshlrev_b32_e32 v130, 2, v66
	ds_bpermute_b32 v55, v130, v35
	ds_bpermute_b32 v54, v130, v34
	v_lshl_add_u64 v[66:67], s[40:41], 1, v[74:75]
	s_waitcnt lgkmcnt(0)
	v_pk_add_f32 v[34:35], v[34:35], v[54:55]
	s_nop 0
	v_pk_fma_f32 v[54:55], v[34:35], s[46:47], v[90:91] op_sel_hi:[1,0,0]
	s_nop 0
	v_mul_f32_e32 v34, 0x4b800000, v55
	v_cmp_gt_f32_e64 s[4:5], s59, v55
	v_cmp_gt_f32_e32 vcc, s59, v54
	s_nop 0
	v_cndmask_b32_e64 v34, v55, v34, s[4:5]
	v_rsq_f32_e32 v34, v34
	s_nop 0
	v_mul_f32_e32 v35, 0x45800000, v34
	v_cndmask_b32_e64 v62, v34, v35, s[4:5]
	v_pk_mul_f32 v[34:35], v[122:123], v[62:63] op_sel_hi:[1,0]
	v_pk_mul_f32 v[64:65], v[64:65], v[62:63] op_sel_hi:[1,0]
	v_pk_mul_f32 v[34:35], v[124:125], v[34:35]
	v_pk_mul_f32 v[64:65], v[120:121], v[64:65]
	v_and_b32_sdwa v55, v35, v113 dst_sel:DWORD dst_unused:UNUSED_PAD src0_sel:WORD_1 src1_sel:DWORD
	v_and_b32_sdwa v63, v34, v113 dst_sel:DWORD dst_unused:UNUSED_PAD src0_sel:WORD_1 src1_sel:DWORD
	v_add3_u32 v34, v34, v63, s75
	v_add3_u32 v35, v35, v55, s75
	v_and_b32_sdwa v55, v65, v113 dst_sel:DWORD dst_unused:UNUSED_PAD src0_sel:WORD_1 src1_sel:DWORD
	v_and_b32_sdwa v63, v64, v113 dst_sel:DWORD dst_unused:UNUSED_PAD src0_sel:WORD_1 src1_sel:DWORD
	v_add3_u32 v55, v65, v55, s75
	v_add3_u32 v63, v64, v63, s75
	v_and_b32_e32 v55, 0xffff0000, v55
	v_and_b32_e32 v63, 0xffff0000, v63
	v_or_b32_sdwa v35, v55, v35 dst_sel:DWORD dst_unused:UNUSED_PAD src0_sel:DWORD src1_sel:WORD_1
	v_or_b32_sdwa v34, v63, v34 dst_sel:DWORD dst_unused:UNUSED_PAD src0_sel:DWORD src1_sel:WORD_1
	global_store_dwordx2 v[66:67], v[34:35], off
	s_waitcnt vmcnt(1)
	v_mov_b32_e32 v92, v136
	v_mov_b32_e32 v93, v137
	v_mov_b32_e32 v94, v138
	v_mov_b32_e32 v95, v139
	v_pk_mul_f32 v[34:35], v[118:119], v[62:63] op_sel_hi:[1,0]
	v_pk_mul_f32 v[60:61], v[60:61], v[62:63] op_sel_hi:[1,0]
	v_mov_b32_e32 v64, v92
	v_mov_b32_e32 v65, v94
	v_pk_mul_f32 v[34:35], v[64:65], v[34:35]
	v_mov_b32_e32 v94, v93
	v_pk_mul_f32 v[60:61], v[94:95], v[60:61]
	v_and_b32_sdwa v55, v35, v113 dst_sel:DWORD dst_unused:UNUSED_PAD src0_sel:WORD_1 src1_sel:DWORD
	v_and_b32_sdwa v63, v34, v113 dst_sel:DWORD dst_unused:UNUSED_PAD src0_sel:WORD_1 src1_sel:DWORD
	v_add3_u32 v34, v34, v63, s75
	v_add3_u32 v35, v35, v55, s75
	v_and_b32_sdwa v55, v61, v113 dst_sel:DWORD dst_unused:UNUSED_PAD src0_sel:WORD_1 src1_sel:DWORD
	v_and_b32_sdwa v63, v60, v113 dst_sel:DWORD dst_unused:UNUSED_PAD src0_sel:WORD_1 src1_sel:DWORD
	v_add3_u32 v55, v61, v55, s75
	v_add3_u32 v60, v60, v63, s75
	v_and_b32_e32 v55, 0xffff0000, v55
	v_and_b32_e32 v60, 0xffff0000, v60
	v_or_b32_sdwa v35, v55, v35 dst_sel:DWORD dst_unused:UNUSED_PAD src0_sel:DWORD src1_sel:WORD_1
	v_or_b32_sdwa v34, v60, v34 dst_sel:DWORD dst_unused:UNUSED_PAD src0_sel:DWORD src1_sel:WORD_1
	global_store_dwordx2 v[66:67], v[34:35], off offset:512
	v_mov_b32_e32 v92, v140
	v_mov_b32_e32 v93, v141
	v_mov_b32_e32 v94, v142
	v_mov_b32_e32 v95, v143
	v_pk_mul_f32 v[34:35], v[98:99], v[62:63] op_sel_hi:[1,0]
	v_pk_mul_f32 v[56:57], v[56:57], v[62:63] op_sel_hi:[1,0]
	v_pk_mul_f32 v[52:53], v[52:53], v[62:63] op_sel_hi:[1,0]
	v_pk_mul_f32 v[50:51], v[50:51], v[62:63] op_sel_hi:[1,0]
	v_pk_mul_f32 v[48:49], v[48:49], v[62:63] op_sel_hi:[1,0]
	v_pk_mul_f32 v[46:47], v[46:47], v[62:63] op_sel_hi:[1,0]
	v_pk_mul_f32 v[44:45], v[44:45], v[62:63] op_sel_hi:[1,0]
	v_pk_mul_f32 v[42:43], v[42:43], v[62:63] op_sel_hi:[1,0]
	v_pk_mul_f32 v[40:41], v[40:41], v[62:63] op_sel_hi:[1,0]
	v_pk_mul_f32 v[38:39], v[38:39], v[62:63] op_sel_hi:[1,0]
	v_pk_mul_f32 v[36:37], v[36:37], v[62:63] op_sel_hi:[1,0]
	v_mov_b32_e32 v60, v92
	v_mov_b32_e32 v61, v94
	v_pk_mul_f32 v[34:35], v[60:61], v[34:35]
	v_mov_b32_e32 v94, v93
	v_pk_mul_f32 v[56:57], v[94:95], v[56:57]
	v_and_b32_sdwa v55, v35, v113 dst_sel:DWORD dst_unused:UNUSED_PAD src0_sel:WORD_1 src1_sel:DWORD
	v_and_b32_sdwa v60, v34, v113 dst_sel:DWORD dst_unused:UNUSED_PAD src0_sel:WORD_1 src1_sel:DWORD
	v_add3_u32 v34, v34, v60, s75
	v_add3_u32 v35, v35, v55, s75
	v_and_b32_sdwa v55, v57, v113 dst_sel:DWORD dst_unused:UNUSED_PAD src0_sel:WORD_1 src1_sel:DWORD
	v_and_b32_sdwa v60, v56, v113 dst_sel:DWORD dst_unused:UNUSED_PAD src0_sel:WORD_1 src1_sel:DWORD
	v_add3_u32 v55, v57, v55, s75
	v_add3_u32 v56, v56, v60, s75
	v_and_b32_e32 v55, 0xffff0000, v55
	v_and_b32_e32 v56, 0xffff0000, v56
	v_or_b32_sdwa v35, v55, v35 dst_sel:DWORD dst_unused:UNUSED_PAD src0_sel:DWORD src1_sel:WORD_1
	v_or_b32_sdwa v34, v56, v34 dst_sel:DWORD dst_unused:UNUSED_PAD src0_sel:DWORD src1_sel:WORD_1
	global_store_dwordx2 v[66:67], v[34:35], off offset:1024
; __device__ __forceinline__ unsigned pk2(float lo, float hi) { return (unsigned)f2bf(lo) | ((unsigned)f2bf(hi) << 16); }
; __device__ __forceinline__ void norm1_rows2(int R0, int lane, const float* x, const float* meta, const float* g, bf16* hn) {
;     ...
; #pragma unroll
;         for (int j = 0; j < 8; ++j) { const f32x4 gg = *(const f32x4*)(g + j * 256 + lane * 4);
;             u32x2 o; o.x = pk2(v[q][j].x * rstd * gg.x, v[q][j].y * rstd * gg.y); o.y = pk2(v[q][j].z * rstd * gg.z, v[q][j].w * rstd * gg.w);
;             *(u32x2*)(hn + (size_t)(R0 + q) * D + j * 256 + lane * 4) = o; } }
	v_mov_b32_e32 v92, v144
	v_mov_b32_e32 v93, v145
	v_mov_b32_e32 v94, v146
	v_mov_b32_e32 v95, v147
	v_pk_mul_f32 v[34:35], v[58:59], v[62:63] op_sel_hi:[1,0]
	v_mov_b32_e32 v56, v92
	v_mov_b32_e32 v57, v94
	v_pk_mul_f32 v[34:35], v[56:57], v[34:35]
	v_mov_b32_e32 v94, v93
	v_pk_mul_f32 v[52:53], v[94:95], v[52:53]
	v_and_b32_sdwa v55, v35, v113 dst_sel:DWORD dst_unused:UNUSED_PAD src0_sel:WORD_1 src1_sel:DWORD
	v_and_b32_sdwa v56, v34, v113 dst_sel:DWORD dst_unused:UNUSED_PAD src0_sel:WORD_1 src1_sel:DWORD
	v_add3_u32 v34, v34, v56, s75
	v_add3_u32 v35, v35, v55, s75
	v_and_b32_sdwa v55, v53, v113 dst_sel:DWORD dst_unused:UNUSED_PAD src0_sel:WORD_1 src1_sel:DWORD
	v_and_b32_sdwa v56, v52, v113 dst_sel:DWORD dst_unused:UNUSED_PAD src0_sel:WORD_1 src1_sel:DWORD
	v_add3_u32 v53, v53, v55, s75
	v_add3_u32 v52, v52, v56, s75
	v_and_b32_e32 v53, 0xffff0000, v53
	v_and_b32_e32 v52, 0xffff0000, v52
	v_or_b32_sdwa v35, v53, v35 dst_sel:DWORD dst_unused:UNUSED_PAD src0_sel:DWORD src1_sel:WORD_1
	v_or_b32_sdwa v34, v52, v34 dst_sel:DWORD dst_unused:UNUSED_PAD src0_sel:DWORD src1_sel:WORD_1
	global_store_dwordx2 v[66:67], v[34:35], off offset:1536
	v_add_co_u32_e64 v34, s[4:5], s73, v68
	s_nop 1
	v_addc_co_u32_e64 v35, s[4:5], 0, v69, s[4:5]
	v_mov_b32_e32 v56, v148
	v_mov_b32_e32 v57, v149
	v_mov_b32_e32 v58, v150
	v_mov_b32_e32 v59, v151
	v_mov_b32_e32 v52, v56
	v_mov_b32_e32 v53, v58
	v_pk_mul_f32 v[50:51], v[52:53], v[50:51]
	v_mov_b32_e32 v58, v57
	v_pk_mul_f32 v[48:49], v[58:59], v[48:49]
	v_and_b32_sdwa v52, v51, v113 dst_sel:DWORD dst_unused:UNUSED_PAD src0_sel:WORD_1 src1_sel:DWORD
	v_and_b32_sdwa v53, v50, v113 dst_sel:DWORD dst_unused:UNUSED_PAD src0_sel:WORD_1 src1_sel:DWORD
	v_add3_u32 v50, v50, v53, s75
	v_add3_u32 v51, v51, v52, s75
	v_and_b32_sdwa v52, v49, v113 dst_sel:DWORD dst_unused:UNUSED_PAD src0_sel:WORD_1 src1_sel:DWORD
	v_and_b32_sdwa v53, v48, v113 dst_sel:DWORD dst_unused:UNUSED_PAD src0_sel:WORD_1 src1_sel:DWORD
	v_add3_u32 v49, v49, v52, s75
	v_add3_u32 v48, v48, v53, s75
	v_and_b32_e32 v49, 0xffff0000, v49
	v_and_b32_e32 v48, 0xffff0000, v48
	v_or_b32_sdwa v49, v49, v51 dst_sel:DWORD dst_unused:UNUSED_PAD src0_sel:DWORD src1_sel:WORD_1
	v_or_b32_sdwa v48, v48, v50 dst_sel:DWORD dst_unused:UNUSED_PAD src0_sel:DWORD src1_sel:WORD_1
	global_store_dwordx2 v[66:67], v[48:49], off offset:2048
	v_mov_b32_e32 v48, v152
	v_mov_b32_e32 v49, v153
	v_mov_b32_e32 v50, v154
	v_mov_b32_e32 v51, v155
	v_mov_b32_e32 v52, v48
	v_mov_b32_e32 v53, v50
	v_pk_mul_f32 v[46:47], v[46:47], v[52:53]
	v_mov_b32_e32 v50, v49
	v_pk_mul_f32 v[44:45], v[44:45], v[50:51]
	v_and_b32_sdwa v48, v47, v113 dst_sel:DWORD dst_unused:UNUSED_PAD src0_sel:WORD_1 src1_sel:DWORD
	v_and_b32_sdwa v49, v46, v113 dst_sel:DWORD dst_unused:UNUSED_PAD src0_sel:WORD_1 src1_sel:DWORD
	v_add3_u32 v46, v46, v49, s75
	v_add3_u32 v47, v47, v48, s75
	v_and_b32_sdwa v48, v45, v113 dst_sel:DWORD dst_unused:UNUSED_PAD src0_sel:WORD_1 src1_sel:DWORD
	v_and_b32_sdwa v49, v44, v113 dst_sel:DWORD dst_unused:UNUSED_PAD src0_sel:WORD_1 src1_sel:DWORD
	v_add3_u32 v45, v45, v48, s75
	v_add3_u32 v44, v44, v49, s75
	v_and_b32_e32 v45, 0xffff0000, v45
	v_and_b32_e32 v44, 0xffff0000, v44
	v_or_b32_sdwa v45, v45, v47 dst_sel:DWORD dst_unused:UNUSED_PAD src0_sel:DWORD src1_sel:WORD_1
	v_or_b32_sdwa v44, v44, v46 dst_sel:DWORD dst_unused:UNUSED_PAD src0_sel:DWORD src1_sel:WORD_1
	global_store_dwordx2 v[66:67], v[44:45], off offset:2560
	v_mov_b32_e32 v44, v156
	v_mov_b32_e32 v45, v157
	v_mov_b32_e32 v46, v158
	v_mov_b32_e32 v47, v159
	v_mov_b32_e32 v48, v44
	v_mov_b32_e32 v49, v46
	v_pk_mul_f32 v[42:43], v[42:43], v[48:49]
	v_mov_b32_e32 v46, v45
	v_pk_mul_f32 v[40:41], v[40:41], v[46:47]
	v_and_b32_sdwa v44, v43, v113 dst_sel:DWORD dst_unused:UNUSED_PAD src0_sel:WORD_1 src1_sel:DWORD
	v_and_b32_sdwa v45, v42, v113 dst_sel:DWORD dst_unused:UNUSED_PAD src0_sel:WORD_1 src1_sel:DWORD
	v_add3_u32 v42, v42, v45, s75
	v_add3_u32 v43, v43, v44, s75
	v_and_b32_sdwa v44, v41, v113 dst_sel:DWORD dst_unused:UNUSED_PAD src0_sel:WORD_1 src1_sel:DWORD
	v_and_b32_sdwa v45, v40, v113 dst_sel:DWORD dst_unused:UNUSED_PAD src0_sel:WORD_1 src1_sel:DWORD
	v_add3_u32 v41, v41, v44, s75
	v_add3_u32 v40, v40, v45, s75
	v_and_b32_e32 v41, 0xffff0000, v41
	v_and_b32_e32 v40, 0xffff0000, v40
	v_or_b32_sdwa v41, v41, v43 dst_sel:DWORD dst_unused:UNUSED_PAD src0_sel:DWORD src1_sel:WORD_1
	v_or_b32_sdwa v40, v40, v42 dst_sel:DWORD dst_unused:UNUSED_PAD src0_sel:DWORD src1_sel:WORD_1
	global_store_dwordx2 v[66:67], v[40:41], off offset:3072
	v_mov_b32_e32 v40, v160
	v_mov_b32_e32 v41, v161
	v_mov_b32_e32 v42, v162
	v_mov_b32_e32 v43, v163
	v_mov_b32_e32 v44, v40
	v_mov_b32_e32 v45, v42
	v_pk_mul_f32 v[38:39], v[38:39], v[44:45]
	v_mov_b32_e32 v42, v41
	v_pk_mul_f32 v[36:37], v[36:37], v[42:43]
	v_and_b32_sdwa v40, v39, v113 dst_sel:DWORD dst_unused:UNUSED_PAD src0_sel:WORD_1 src1_sel:DWORD
	v_and_b32_sdwa v41, v38, v113 dst_sel:DWORD dst_unused:UNUSED_PAD src0_sel:WORD_1 src1_sel:DWORD
	v_add3_u32 v38, v38, v41, s75
	v_add3_u32 v39, v39, v40, s75
	v_and_b32_sdwa v40, v37, v113 dst_sel:DWORD dst_unused:UNUSED_PAD src0_sel:WORD_1 src1_sel:DWORD
	v_and_b32_sdwa v41, v36, v113 dst_sel:DWORD dst_unused:UNUSED_PAD src0_sel:WORD_1 src1_sel:DWORD
	v_add3_u32 v37, v37, v40, s75
	v_add3_u32 v36, v36, v41, s75
	v_and_b32_e32 v37, 0xffff0000, v37
	v_and_b32_e32 v36, 0xffff0000, v36
	v_or_b32_sdwa v37, v37, v39 dst_sel:DWORD dst_unused:UNUSED_PAD src0_sel:DWORD src1_sel:WORD_1
	v_or_b32_sdwa v36, v36, v38 dst_sel:DWORD dst_unused:UNUSED_PAD src0_sel:DWORD src1_sel:WORD_1
	global_store_dwordx2 v[66:67], v[36:37], off offset:3584
; __device__ __forceinline__ unsigned pk2(float lo, float hi) { return (unsigned)f2bf(lo) | ((unsigned)f2bf(hi) << 16); }
; __device__ __forceinline__ void norm1_rows2(int R0, int lane, const float* x, const float* meta, const float* g, bf16* hn) {
;     ...
;     for (int q = 0; q < 2; ++q) { const float rstd = rsqrtf(wave_sum(ss[q]) * (1.f / D) + EPS);
; #pragma unroll
;         for (int j = 0; j < 8; ++j) { const f32x4 gg = *(const f32x4*)(g + j * 256 + lane * 4);
;             u32x2 o; o.x = pk2(v[q][j].x * rstd * gg.x, v[q][j].y * rstd * gg.y); o.y = pk2(v[q][j].z * rstd * gg.z, v[q][j].w * rstd * gg.w);
;             *(u32x2*)(hn + (size_t)(R0 + q) * D + j * 256 + lane * 4) = o; } }
	v_mov_b32_e32 v40, v132
	v_mov_b32_e32 v41, v133
	v_mov_b32_e32 v42, v134
	v_mov_b32_e32 v43, v135
	v_mul_f32_e32 v36, 0x4b800000, v54
	v_cndmask_b32_e32 v36, v54, v36, vcc
	v_rsq_f32_e32 v36, v36
	v_mov_b32_e32 v45, v32
	v_mov_b32_e32 v32, v31
	v_mov_b32_e32 v44, v30
	v_mul_f32_e32 v37, 0x45800000, v36
	v_cndmask_b32_e32 v38, v36, v37, vcc
	v_pk_mul_f32 v[30:31], v[32:33], v[38:39] op_sel_hi:[1,0]
	v_pk_mul_f32 v[44:45], v[44:45], v[38:39] op_sel_hi:[1,0]
	v_lshl_add_u64 v[36:37], s[8:9], 1, v[74:75]
	v_mov_b32_e32 v47, v42
	v_mov_b32_e32 v42, v41
	v_mov_b32_e32 v46, v40
	v_pk_mul_f32 v[30:31], v[42:43], v[30:31]
	v_pk_mul_f32 v[44:45], v[46:47], v[44:45]
	v_and_b32_sdwa v39, v31, v113 dst_sel:DWORD dst_unused:UNUSED_PAD src0_sel:WORD_1 src1_sel:DWORD
	v_and_b32_sdwa v40, v30, v113 dst_sel:DWORD dst_unused:UNUSED_PAD src0_sel:WORD_1 src1_sel:DWORD
	v_and_b32_sdwa v32, v45, v113 dst_sel:DWORD dst_unused:UNUSED_PAD src0_sel:WORD_1 src1_sel:DWORD
	v_and_b32_sdwa v33, v44, v113 dst_sel:DWORD dst_unused:UNUSED_PAD src0_sel:WORD_1 src1_sel:DWORD
	v_add3_u32 v31, v31, v39, s75
	v_add3_u32 v30, v30, v40, s75
	v_add3_u32 v33, v44, v33, s75
	v_add3_u32 v32, v45, v32, s75
	v_and_b32_e32 v31, 0xffff0000, v31
	v_and_b32_e32 v30, 0xffff0000, v30
	v_or_b32_sdwa v31, v31, v32 dst_sel:DWORD dst_unused:UNUSED_PAD src0_sel:DWORD src1_sel:WORD_1
	v_or_b32_sdwa v30, v30, v33 dst_sel:DWORD dst_unused:UNUSED_PAD src0_sel:DWORD src1_sel:WORD_1
	global_store_dwordx2 v[36:37], v[30:31], off
	v_mov_b32_e32 v30, v136
	v_mov_b32_e32 v31, v137
	v_mov_b32_e32 v32, v138
	v_mov_b32_e32 v33, v139
	v_mov_b32_e32 v41, v28
	v_mov_b32_e32 v28, v27
	v_mov_b32_e32 v40, v26
	v_pk_mul_f32 v[26:27], v[28:29], v[38:39] op_sel_hi:[1,0]
	v_pk_mul_f32 v[40:41], v[40:41], v[38:39] op_sel_hi:[1,0]
	v_mov_b32_e32 v43, v32
	v_mov_b32_e32 v32, v31
	v_mov_b32_e32 v42, v30
	v_pk_mul_f32 v[26:27], v[32:33], v[26:27]
	v_pk_mul_f32 v[40:41], v[42:43], v[40:41]
	v_and_b32_sdwa v30, v27, v113 dst_sel:DWORD dst_unused:UNUSED_PAD src0_sel:WORD_1 src1_sel:DWORD
	v_and_b32_sdwa v31, v26, v113 dst_sel:DWORD dst_unused:UNUSED_PAD src0_sel:WORD_1 src1_sel:DWORD
	v_and_b32_sdwa v28, v41, v113 dst_sel:DWORD dst_unused:UNUSED_PAD src0_sel:WORD_1 src1_sel:DWORD
	v_and_b32_sdwa v29, v40, v113 dst_sel:DWORD dst_unused:UNUSED_PAD src0_sel:WORD_1 src1_sel:DWORD
	v_add3_u32 v27, v27, v30, s75
	v_add3_u32 v26, v26, v31, s75
	v_add3_u32 v29, v40, v29, s75
	v_add3_u32 v28, v41, v28, s75
	v_and_b32_e32 v27, 0xffff0000, v27
	v_and_b32_e32 v26, 0xffff0000, v26
	v_or_b32_sdwa v27, v27, v28 dst_sel:DWORD dst_unused:UNUSED_PAD src0_sel:DWORD src1_sel:WORD_1
	v_or_b32_sdwa v26, v26, v29 dst_sel:DWORD dst_unused:UNUSED_PAD src0_sel:DWORD src1_sel:WORD_1
	global_store_dwordx2 v[36:37], v[26:27], off offset:512
	v_mov_b32_e32 v26, v140
	v_mov_b32_e32 v27, v141
	v_mov_b32_e32 v28, v142
	v_mov_b32_e32 v29, v143
	v_mov_b32_e32 v31, v24
	v_mov_b32_e32 v24, v23
	v_mov_b32_e32 v30, v22
	v_pk_mul_f32 v[22:23], v[24:25], v[38:39] op_sel_hi:[1,0]
	v_pk_mul_f32 v[30:31], v[30:31], v[38:39] op_sel_hi:[1,0]
	v_mov_b32_e32 v33, v28
	v_mov_b32_e32 v28, v27
	v_mov_b32_e32 v32, v26
	v_pk_mul_f32 v[22:23], v[28:29], v[22:23]
	v_pk_mul_f32 v[30:31], v[32:33], v[30:31]
	v_and_b32_sdwa v26, v23, v113 dst_sel:DWORD dst_unused:UNUSED_PAD src0_sel:WORD_1 src1_sel:DWORD
	v_and_b32_sdwa v27, v22, v113 dst_sel:DWORD dst_unused:UNUSED_PAD src0_sel:WORD_1 src1_sel:DWORD
	v_and_b32_sdwa v24, v31, v113 dst_sel:DWORD dst_unused:UNUSED_PAD src0_sel:WORD_1 src1_sel:DWORD
	v_and_b32_sdwa v25, v30, v113 dst_sel:DWORD dst_unused:UNUSED_PAD src0_sel:WORD_1 src1_sel:DWORD
	v_add3_u32 v23, v23, v26, s75
	v_add3_u32 v22, v22, v27, s75
	v_add3_u32 v25, v30, v25, s75
	v_add3_u32 v24, v31, v24, s75
	v_and_b32_e32 v23, 0xffff0000, v23
	v_and_b32_e32 v22, 0xffff0000, v22
	v_or_b32_sdwa v23, v23, v24 dst_sel:DWORD dst_unused:UNUSED_PAD src0_sel:DWORD src1_sel:WORD_1
	v_or_b32_sdwa v22, v22, v25 dst_sel:DWORD dst_unused:UNUSED_PAD src0_sel:DWORD src1_sel:WORD_1
	global_store_dwordx2 v[36:37], v[22:23], off offset:1024
	v_mov_b32_e32 v22, v144
	v_mov_b32_e32 v23, v145
	v_mov_b32_e32 v24, v146
	v_mov_b32_e32 v25, v147
	v_mov_b32_e32 v27, v20
	v_mov_b32_e32 v20, v19
	v_mov_b32_e32 v26, v18
	v_pk_mul_f32 v[18:19], v[20:21], v[38:39] op_sel_hi:[1,0]
	v_pk_mul_f32 v[26:27], v[26:27], v[38:39] op_sel_hi:[1,0]
	v_mov_b32_e32 v29, v24
	v_mov_b32_e32 v24, v23
	v_mov_b32_e32 v28, v22
	v_pk_mul_f32 v[18:19], v[24:25], v[18:19]
	v_pk_mul_f32 v[26:27], v[28:29], v[26:27]
	v_and_b32_sdwa v22, v19, v113 dst_sel:DWORD dst_unused:UNUSED_PAD src0_sel:WORD_1 src1_sel:DWORD
	v_and_b32_sdwa v23, v18, v113 dst_sel:DWORD dst_unused:UNUSED_PAD src0_sel:WORD_1 src1_sel:DWORD
	v_and_b32_sdwa v20, v27, v113 dst_sel:DWORD dst_unused:UNUSED_PAD src0_sel:WORD_1 src1_sel:DWORD
	v_and_b32_sdwa v21, v26, v113 dst_sel:DWORD dst_unused:UNUSED_PAD src0_sel:WORD_1 src1_sel:DWORD
	v_add3_u32 v19, v19, v22, s75
	v_add3_u32 v18, v18, v23, s75
	v_add3_u32 v21, v26, v21, s75
	v_add3_u32 v20, v27, v20, s75
	v_and_b32_e32 v19, 0xffff0000, v19
	v_and_b32_e32 v18, 0xffff0000, v18
	v_or_b32_sdwa v19, v19, v20 dst_sel:DWORD dst_unused:UNUSED_PAD src0_sel:DWORD src1_sel:WORD_1
; __device__ __forceinline__ unsigned pk2(float lo, float hi) { return (unsigned)f2bf(lo) | ((unsigned)f2bf(hi) << 16); }
; __device__ __forceinline__ void norm1_rows2(int R0, int lane, const float* x, const float* meta, const float* g, bf16* hn) {
;     ...
; #pragma unroll
;         for (int j = 0; j < 8; ++j) { const f32x4 gg = *(const f32x4*)(g + j * 256 + lane * 4);
;             u32x2 o; o.x = pk2(v[q][j].x * rstd * gg.x, v[q][j].y * rstd * gg.y); o.y = pk2(v[q][j].z * rstd * gg.z, v[q][j].w * rstd * gg.w);
;             *(u32x2*)(hn + (size_t)(R0 + q) * D + j * 256 + lane * 4) = o; } }
	v_or_b32_sdwa v18, v18, v21 dst_sel:DWORD dst_unused:UNUSED_PAD src0_sel:DWORD src1_sel:WORD_1
	global_store_dwordx2 v[36:37], v[18:19], off offset:1536
	v_mov_b32_e32 v18, v148
	v_mov_b32_e32 v19, v149
	v_mov_b32_e32 v20, v150
	v_mov_b32_e32 v21, v151
	v_mov_b32_e32 v23, v16
	v_mov_b32_e32 v16, v15
	v_mov_b32_e32 v22, v14
	v_pk_mul_f32 v[14:15], v[16:17], v[38:39] op_sel_hi:[1,0]
	v_pk_mul_f32 v[22:23], v[22:23], v[38:39] op_sel_hi:[1,0]
	v_mov_b32_e32 v25, v20
	v_mov_b32_e32 v20, v19
	v_mov_b32_e32 v24, v18
	v_pk_mul_f32 v[14:15], v[20:21], v[14:15]
	v_pk_mul_f32 v[22:23], v[24:25], v[22:23]
	v_and_b32_sdwa v18, v15, v113 dst_sel:DWORD dst_unused:UNUSED_PAD src0_sel:WORD_1 src1_sel:DWORD
	v_and_b32_sdwa v19, v14, v113 dst_sel:DWORD dst_unused:UNUSED_PAD src0_sel:WORD_1 src1_sel:DWORD
	v_and_b32_sdwa v16, v23, v113 dst_sel:DWORD dst_unused:UNUSED_PAD src0_sel:WORD_1 src1_sel:DWORD
	v_and_b32_sdwa v17, v22, v113 dst_sel:DWORD dst_unused:UNUSED_PAD src0_sel:WORD_1 src1_sel:DWORD
	v_add3_u32 v15, v15, v18, s75
	v_add3_u32 v14, v14, v19, s75
	v_add3_u32 v17, v22, v17, s75
	v_add3_u32 v16, v23, v16, s75
	v_and_b32_e32 v15, 0xffff0000, v15
	v_and_b32_e32 v14, 0xffff0000, v14
	v_or_b32_sdwa v15, v15, v16 dst_sel:DWORD dst_unused:UNUSED_PAD src0_sel:DWORD src1_sel:WORD_1
	v_or_b32_sdwa v14, v14, v17 dst_sel:DWORD dst_unused:UNUSED_PAD src0_sel:DWORD src1_sel:WORD_1
	global_store_dwordx2 v[36:37], v[14:15], off offset:2048
	v_mov_b32_e32 v14, v152
	v_mov_b32_e32 v15, v153
	v_mov_b32_e32 v16, v154
	v_mov_b32_e32 v17, v155
	v_mov_b32_e32 v19, v12
	v_mov_b32_e32 v12, v11
	v_mov_b32_e32 v18, v10
	v_pk_mul_f32 v[10:11], v[12:13], v[38:39] op_sel_hi:[1,0]
	v_pk_mul_f32 v[18:19], v[18:19], v[38:39] op_sel_hi:[1,0]
	v_mov_b32_e32 v21, v16
	v_mov_b32_e32 v16, v15
	v_mov_b32_e32 v20, v14
	v_pk_mul_f32 v[10:11], v[10:11], v[16:17]
	v_pk_mul_f32 v[18:19], v[18:19], v[20:21]
	v_and_b32_sdwa v14, v11, v113 dst_sel:DWORD dst_unused:UNUSED_PAD src0_sel:WORD_1 src1_sel:DWORD
	v_and_b32_sdwa v15, v10, v113 dst_sel:DWORD dst_unused:UNUSED_PAD src0_sel:WORD_1 src1_sel:DWORD
	v_and_b32_sdwa v12, v19, v113 dst_sel:DWORD dst_unused:UNUSED_PAD src0_sel:WORD_1 src1_sel:DWORD
	v_and_b32_sdwa v13, v18, v113 dst_sel:DWORD dst_unused:UNUSED_PAD src0_sel:WORD_1 src1_sel:DWORD
	v_add3_u32 v11, v11, v14, s75
	v_add3_u32 v10, v10, v15, s75
	v_add3_u32 v13, v18, v13, s75
	v_add3_u32 v12, v19, v12, s75
	v_and_b32_e32 v11, 0xffff0000, v11
	v_and_b32_e32 v10, 0xffff0000, v10
	v_or_b32_sdwa v11, v11, v12 dst_sel:DWORD dst_unused:UNUSED_PAD src0_sel:DWORD src1_sel:WORD_1
	v_or_b32_sdwa v10, v10, v13 dst_sel:DWORD dst_unused:UNUSED_PAD src0_sel:DWORD src1_sel:WORD_1
	global_store_dwordx2 v[36:37], v[10:11], off offset:2560
	v_mov_b32_e32 v10, v156
	v_mov_b32_e32 v11, v157
	v_mov_b32_e32 v12, v158
	v_mov_b32_e32 v13, v159
	v_mov_b32_e32 v15, v8
	v_mov_b32_e32 v8, v7
	v_mov_b32_e32 v14, v6
	v_pk_mul_f32 v[6:7], v[8:9], v[38:39] op_sel_hi:[1,0]
	v_pk_mul_f32 v[14:15], v[14:15], v[38:39] op_sel_hi:[1,0]
	v_mov_b32_e32 v17, v12
	v_mov_b32_e32 v12, v11
	v_mov_b32_e32 v16, v10
	v_pk_mul_f32 v[6:7], v[6:7], v[12:13]
	v_pk_mul_f32 v[14:15], v[14:15], v[16:17]
	v_and_b32_sdwa v10, v7, v113 dst_sel:DWORD dst_unused:UNUSED_PAD src0_sel:WORD_1 src1_sel:DWORD
	v_and_b32_sdwa v11, v6, v113 dst_sel:DWORD dst_unused:UNUSED_PAD src0_sel:WORD_1 src1_sel:DWORD
	v_and_b32_sdwa v8, v15, v113 dst_sel:DWORD dst_unused:UNUSED_PAD src0_sel:WORD_1 src1_sel:DWORD
	v_and_b32_sdwa v9, v14, v113 dst_sel:DWORD dst_unused:UNUSED_PAD src0_sel:WORD_1 src1_sel:DWORD
	v_add3_u32 v7, v7, v10, s75
	v_add3_u32 v6, v6, v11, s75
	v_add3_u32 v9, v14, v9, s75
	v_add3_u32 v8, v15, v8, s75
	v_and_b32_e32 v7, 0xffff0000, v7
	v_and_b32_e32 v6, 0xffff0000, v6
	v_or_b32_sdwa v7, v7, v8 dst_sel:DWORD dst_unused:UNUSED_PAD src0_sel:DWORD src1_sel:WORD_1
	v_or_b32_sdwa v6, v6, v9 dst_sel:DWORD dst_unused:UNUSED_PAD src0_sel:DWORD src1_sel:WORD_1
	global_store_dwordx2 v[36:37], v[6:7], off offset:3072
	v_mov_b32_e32 v6, v160
	v_mov_b32_e32 v7, v161
	v_mov_b32_e32 v8, v162
	v_mov_b32_e32 v9, v163
	v_mov_b32_e32 v11, v4
	v_mov_b32_e32 v4, v3
	v_mov_b32_e32 v10, v2
	v_pk_mul_f32 v[2:3], v[4:5], v[38:39] op_sel_hi:[1,0]
	v_pk_mul_f32 v[10:11], v[10:11], v[38:39] op_sel_hi:[1,0]
	v_mov_b32_e32 v13, v8
	v_mov_b32_e32 v8, v7
	v_mov_b32_e32 v12, v6
	v_pk_mul_f32 v[2:3], v[2:3], v[8:9]
	v_pk_mul_f32 v[10:11], v[10:11], v[12:13]
	v_and_b32_sdwa v6, v3, v113 dst_sel:DWORD dst_unused:UNUSED_PAD src0_sel:WORD_1 src1_sel:DWORD
	v_and_b32_sdwa v7, v2, v113 dst_sel:DWORD dst_unused:UNUSED_PAD src0_sel:WORD_1 src1_sel:DWORD
	v_and_b32_sdwa v4, v11, v113 dst_sel:DWORD dst_unused:UNUSED_PAD src0_sel:WORD_1 src1_sel:DWORD
	v_and_b32_sdwa v5, v10, v113 dst_sel:DWORD dst_unused:UNUSED_PAD src0_sel:WORD_1 src1_sel:DWORD
	v_add3_u32 v3, v3, v6, s75
	v_add3_u32 v2, v2, v7, s75
	v_add3_u32 v5, v10, v5, s75
	v_add3_u32 v4, v11, v4, s75
	v_and_b32_e32 v3, 0xffff0000, v3
	v_and_b32_e32 v2, 0xffff0000, v2
	v_or_b32_sdwa v3, v3, v4 dst_sel:DWORD dst_unused:UNUSED_PAD src0_sel:DWORD src1_sel:WORD_1
	v_or_b32_sdwa v2, v2, v5 dst_sel:DWORD dst_unused:UNUSED_PAD src0_sel:DWORD src1_sel:WORD_1
	global_store_dwordx2 v[36:37], v[2:3], off offset:3584
